# baseline (speedup 1.0000x reference)
.LBB1_15:
	s_cmp_gt_i32 s77, 7
	s_cselect_b64 s[52:53], -1, 0
	s_lshl_b32 s4, s77, 2
	s_add_i32 s78, s4, s66
	s_or_b32 s37, s4, s62
	s_lshr_b32 s4, s27, 8
	s_and_b32 s4, s4, 0x7ff8
	v_and_b32_e32 v147, 64, v198
	s_add_i32 s10, s4, s78
	s_lshr_b32 s4, s27, 6
	v_xor_b32_e32 v146, 16, v198
	v_add_u32_e32 v206, 64, v147
	s_and_b32 s4, s4, 0x7fe0
	v_cmp_lt_i32_e32 vcc, v146, v206
	s_add_i32 s54, s4, s37
	s_cmp_lt_i32 s77, 8
	v_cndmask_b32_e32 v146, v198, v146, vcc
	v_lshlrev_b32_e32 v201, 2, v146
	v_mul_f32_e32 v146, v127, v127
	v_mul_f32_e32 v147, v129, v129
	s_cselect_b64 s[6:7], -1, 0
	v_fmac_f32_e32 v146, v126, v126
	v_fmac_f32_e32 v147, v128, v128
	s_and_b64 s[4:5], s[6:7], exec
	v_add_f32_e32 v153, v146, v147
	v_pk_mul_f32 v[146:147], v[124:125], v[124:125]
	v_pk_mul_f32 v[148:149], v[122:123], v[122:123]
	s_cselect_b32 s9, s23, s25
	s_cselect_b32 s8, s22, s24
	v_and_b32_e32 v152, 0x7cf, v199
	v_mov_b32_e32 v150, v146
	v_mov_b32_e32 v151, v148
	v_mov_b32_e32 v148, v147
	global_load_dwordx4 v[138:141], v194, s[8:9] offset:16
	global_load_dwordx4 v[142:145], v194, s[8:9]
	global_load_dwordx4 v[130:133], v194, s[8:9] offset:144
	global_load_dwordx4 v[134:137], v194, s[8:9] offset:128
	v_pk_add_f32 v[146:147], v[150:151], v[148:149]
	v_lshlrev_b32_e32 v170, 7, v152
	v_add_f32_e32 v147, v153, v147
	v_lshl_add_u64 v[158:159], v[172:173], 0, v[170:171]
	v_lshl_add_u64 v[150:151], v[174:175], 0, v[170:171]
	v_add_f32_e32 v207, v146, v147
	global_load_dwordx4 v[146:149], v[150:151], off offset:16
	s_nop 0
	global_load_dwordx4 v[150:153], v[150:151], off
	s_nop 0
	global_load_dwordx4 v[154:157], v[158:159], off offset:16
	s_nop 0
	global_load_dwordx4 v[158:161], v[158:159], off
	v_mov_b32_e32 v247, 0
	v_and_b32_e32 v242, 0x7cf, v199
	v_lshlrev_b32_e32 v242, 7, v242
	v_add_u32_e32 v246, 0x800, v242
	v_lshl_add_u64 v[244:245], v[172:173], 0, v[246:247]
	global_load_dword v243, v[244:245], off
	v_lshl_add_u64 v[244:245], v[174:175], 0, v[246:247]
	global_load_dword v243, v[244:245], off
	v_add_u32_e32 v246, 0x1000, v242
	v_lshl_add_u64 v[244:245], v[172:173], 0, v[246:247]
	global_load_dword v243, v[244:245], off
	v_lshl_add_u64 v[244:245], v[174:175], 0, v[246:247]
	global_load_dword v243, v[244:245], off
	v_add_u32_e32 v246, 0x1800, v242
	v_lshl_add_u64 v[244:245], v[172:173], 0, v[246:247]
	global_load_dword v243, v[244:245], off
	v_lshl_add_u64 v[244:245], v[174:175], 0, v[246:247]
	global_load_dword v243, v[244:245], off
	v_pk_mul_f32 v[184:185], v[112:113], v[112:113]
	v_pk_mul_f32 v[202:203], v[110:111], v[110:111]
	v_mov_b32_e32 v204, v184
	v_mov_b32_e32 v205, v202
	v_mov_b32_e32 v202, v185
	v_pk_add_f32 v[184:185], v[204:205], v[202:203]
	v_pk_mul_f32 v[202:203], v[106:107], v[106:107]
	v_add_f32_e32 v170, v207, v185
	v_add_f32_e32 v170, v184, v170
	v_pk_mul_f32 v[184:185], v[108:109], v[108:109]
	v_mov_b32_e32 v205, v202
	v_mov_b32_e32 v204, v184
	v_mov_b32_e32 v202, v185
	v_pk_add_f32 v[184:185], v[204:205], v[202:203]
	v_cndmask_b32_e64 v200, 1.0, v197, s[6:7]
	v_add_f32_e32 v170, v185, v170
	v_add_f32_e32 v170, v184, v170
	ds_bpermute_b32 v184, v201, v170
	v_xor_b32_e32 v185, 32, v198
	v_cmp_lt_i32_e32 vcc, v185, v206
	s_cselect_b32 s55, s17, s19
	v_or_b32_e32 v229, 16, v199
	v_cndmask_b32_e32 v185, v198, v185, vcc
	v_lshlrev_b32_e32 v202, 2, v185
	s_waitcnt lgkmcnt(0)
	v_add_f32_e32 v170, v170, v184
	ds_bpermute_b32 v184, v202, v170
	s_waitcnt lgkmcnt(0)
	v_add_f32_e32 v170, v170, v184
	v_fmamk_f32 v170, v170, 0x3c800000, v195
	v_mul_f32_e32 v184, 0x4f800000, v170
	v_cmp_gt_f32_e32 vcc, s70, v170
	s_nop 1
	v_cndmask_b32_e32 v170, v170, v184, vcc
	v_sqrt_f32_e32 v184, v170
	s_nop 0
	v_add_u32_e32 v185, -1, v184
	v_fma_f32 v203, -v185, v184, v170
	v_cmp_ge_f32_e64 s[8:9], 0, v203
	v_add_u32_e32 v203, 1, v184
	s_nop 0
	v_cndmask_b32_e64 v185, v184, v185, s[8:9]
	v_fma_f32 v184, -v203, v184, v170
	v_cmp_lt_f32_e64 s[8:9], 0, v184
	s_nop 1
	v_cndmask_b32_e64 v184, v185, v203, s[8:9]
	v_mul_f32_e32 v185, 0x37800000, v184
	v_cndmask_b32_e32 v184, v184, v185, vcc
	v_cmp_class_f32_e32 vcc, v170, v196
	v_lshl_or_b32 v203, s10, 17, v187
	v_lshl_or_b32 v185, s54, 17, v188
	v_cndmask_b32_e32 v170, v184, v170, vcc
	v_div_scale_f32 v184, s[8:9], v170, v170, v200
	v_rcp_f32_e32 v204, v184
	s_cselect_b32 s54, s16, s18
	s_cselect_b32 s10, s72, 0x1000
	v_fma_f32 v205, -v184, v204, 1.0
	v_fmac_f32_e32 v204, v205, v204
	v_div_scale_f32 v205, vcc, v200, v170, v200
	v_mul_f32_e32 v206, v205, v204
	v_fma_f32 v207, -v184, v206, v205
	v_fmac_f32_e32 v206, v207, v204
	v_fma_f32 v184, -v184, v206, v205
	v_div_fmas_f32 v184, v184, v204, v206
	v_div_fixup_f32 v170, v184, v170, v200
	v_pk_mul_f32 v[216:217], v[106:107], v[170:171] op_sel_hi:[1,0]
	v_pk_mul_f32 v[210:211], v[122:123], v[170:171] op_sel_hi:[1,0]
	s_waitcnt vmcnt(6)
	v_pk_mul_f32 v[216:217], v[130:131], v[216:217]
	v_pk_mul_f32 v[210:211], v[138:139], v[210:211]
	v_pk_mul_f32 v[224:225], v[146:147], v[216:217]
	v_pk_mul_f32 v[212:213], v[110:111], v[170:171] op_sel_hi:[1,0]
	v_pk_fma_f32 v[224:225], v[154:155], v[210:211], v[224:225] neg_lo:[0,0,1] neg_hi:[0,0,1]
	v_pk_mul_f32 v[154:155], v[154:155], v[216:217]
	v_pk_mul_f32 v[214:215], v[112:113], v[170:171] op_sel_hi:[1,0]
	v_pk_mul_f32 v[218:219], v[108:109], v[170:171] op_sel_hi:[1,0]
	v_pk_fma_f32 v[154:155], v[146:147], v[210:211], v[154:155]
	v_lshlrev_b32_e32 v146, 6, v199
	v_pk_mul_f32 v[204:205], v[128:129], v[170:171] op_sel_hi:[1,0]
	v_pk_mul_f32 v[206:207], v[126:127], v[170:171] op_sel_hi:[1,0]
	v_pk_mul_f32 v[208:209], v[124:125], v[170:171] op_sel_hi:[1,0]
	v_pk_mul_f32 v[214:215], v[136:137], v[214:215]
	v_pk_mul_f32 v[212:213], v[134:135], v[212:213]
	v_pk_mul_f32 v[218:219], v[132:133], v[218:219]
	v_cndmask_b32_e64 v184, v203, v185, s[6:7]
	v_and_b32_e32 v228, 0x1f000, v146
	v_pk_mul_f32 v[206:207], v[142:143], v[206:207]
	v_pk_mul_f32 v[204:205], v[144:145], v[204:205]
	v_pk_mul_f32 v[208:209], v[140:141], v[208:209]
	v_pk_mul_f32 v[220:221], v[150:151], v[212:213]
	v_pk_mul_f32 v[222:223], v[152:153], v[214:215]
	v_pk_mul_f32 v[226:227], v[148:149], v[218:219]
	v_or3_b32 v146, v228, v189, v184
	v_pk_fma_f32 v[222:223], v[160:161], v[204:205], v[222:223] neg_lo:[0,0,1] neg_hi:[0,0,1]
	v_pk_fma_f32 v[220:221], v[158:159], v[206:207], v[220:221] neg_lo:[0,0,1] neg_hi:[0,0,1]
	v_pk_fma_f32 v[226:227], v[156:157], v[208:209], v[226:227] neg_lo:[0,0,1] neg_hi:[0,0,1]
	v_pk_mul_f32 v[158:159], v[158:159], v[212:213]
	v_pk_mul_f32 v[160:161], v[160:161], v[214:215]
	v_pk_mul_f32 v[156:157], v[156:157], v[218:219]
	v_ashrrev_i32_e32 v147, 31, v146
	v_pk_fma_f32 v[152:153], v[152:153], v[204:205], v[160:161]
	v_pk_fma_f32 v[150:151], v[150:151], v[206:207], v[158:159]
	v_pk_fma_f32 v[156:157], v[148:149], v[208:209], v[156:157]
	v_lshl_add_u64 v[158:159], v[146:147], 1, s[54:55]
	v_cvt_pk_f16_f32 v146, v220, v221
	v_cvt_pk_f16_f32 v147, v222, v223
	v_cvt_pk_f16_f32 v148, v224, v225
	v_cvt_pk_f16_f32 v149, v226, v227
	v_cvt_pk_f16_f32 v150, v150, v151
	v_cvt_pk_f16_f32 v151, v152, v153
	v_cvt_pk_f16_f32 v152, v154, v155
	v_cvt_pk_f16_f32 v153, v156, v157
	global_store_dwordx4 v[158:159], v[146:149], off sc1
	v_pk_mul_f32 v[204:205], v[96:97], v[96:97]
	v_pk_mul_f32 v[206:207], v[94:95], v[94:95]
	v_lshl_add_u64 v[146:147], v[158:159], 0, s[10:11]
	global_store_dwordx4 v[146:147], v[150:153], off sc1
	v_mul_f32_e32 v146, v119, v119
	v_mul_f32_e32 v147, v121, v121
	v_fmac_f32_e32 v146, v118, v118
	v_fmac_f32_e32 v147, v120, v120
	v_add_f32_e32 v153, v146, v147
	v_pk_mul_f32 v[146:147], v[116:117], v[116:117]
	v_pk_mul_f32 v[148:149], v[114:115], v[114:115]
	v_bitop3_b32 v152, v199, s73, 16 bitop3:0xc8
	v_mov_b32_e32 v150, v146
	v_mov_b32_e32 v151, v148
	v_mov_b32_e32 v148, v147
	v_pk_add_f32 v[146:147], v[150:151], v[148:149]
	v_lshlrev_b32_e32 v170, 7, v152
	v_add_f32_e32 v147, v153, v147
	v_lshl_add_u64 v[158:159], v[172:173], 0, v[170:171]
	v_lshl_add_u64 v[150:151], v[174:175], 0, v[170:171]
	v_add_f32_e32 v210, v146, v147
	global_load_dwordx4 v[146:149], v[150:151], off offset:16
	s_nop 0
	global_load_dwordx4 v[150:153], v[150:151], off
	s_nop 0
	global_load_dwordx4 v[154:157], v[158:159], off offset:16
	s_nop 0
	global_load_dwordx4 v[158:161], v[158:159], off
	v_mov_b32_e32 v208, v204
	v_mov_b32_e32 v209, v206
	v_mov_b32_e32 v206, v205
	v_pk_add_f32 v[204:205], v[208:209], v[206:207]
	v_pk_mul_f32 v[206:207], v[90:91], v[90:91]
	v_add_f32_e32 v170, v210, v205
	v_add_f32_e32 v170, v204, v170
	v_pk_mul_f32 v[204:205], v[92:93], v[92:93]
	v_mov_b32_e32 v209, v206
	v_mov_b32_e32 v208, v204
	v_mov_b32_e32 v206, v205
	v_pk_add_f32 v[204:205], v[208:209], v[206:207]
	s_nop 0
	v_add_f32_e32 v170, v205, v170
	v_add_f32_e32 v170, v204, v170
	ds_bpermute_b32 v204, v201, v170
	s_waitcnt lgkmcnt(0)
	v_add_f32_e32 v170, v170, v204
	ds_bpermute_b32 v204, v202, v170
	s_waitcnt lgkmcnt(0)
	v_add_f32_e32 v170, v170, v204
	v_fmamk_f32 v170, v170, 0x3c800000, v195
	v_mul_f32_e32 v204, 0x4f800000, v170
	v_cmp_gt_f32_e32 vcc, s70, v170
	s_nop 1
	v_cndmask_b32_e32 v170, v170, v204, vcc
	v_sqrt_f32_e32 v204, v170
	s_nop 0
	v_add_u32_e32 v205, -1, v204
	v_fma_f32 v206, -v205, v204, v170
	v_cmp_ge_f32_e64 s[8:9], 0, v206
	v_add_u32_e32 v206, 1, v204
	s_nop 0
	v_cndmask_b32_e64 v205, v204, v205, s[8:9]
	v_fma_f32 v204, -v206, v204, v170
	v_cmp_lt_f32_e64 s[8:9], 0, v204
	s_nop 1
	v_cndmask_b32_e64 v204, v205, v206, s[8:9]
	v_mul_f32_e32 v205, 0x37800000, v204
	v_cndmask_b32_e32 v204, v204, v205, vcc
	v_cmp_class_f32_e32 vcc, v170, v196
	s_nop 1
	v_cndmask_b32_e32 v170, v204, v170, vcc
	v_div_scale_f32 v204, s[8:9], v170, v170, v200
	v_rcp_f32_e32 v205, v204
	s_mov_b64 s[8:9], -1
	v_fma_f32 v206, -v204, v205, 1.0
	v_fmac_f32_e32 v205, v206, v205
	v_div_scale_f32 v206, vcc, v200, v170, v200
	v_mul_f32_e32 v207, v206, v205
	v_fma_f32 v208, -v204, v207, v206
	v_fmac_f32_e32 v207, v208, v205
	v_fma_f32 v204, -v204, v207, v206
	v_div_fmas_f32 v204, v204, v205, v207
	v_div_fixup_f32 v170, v204, v170, v200
	v_pk_mul_f32 v[216:217], v[90:91], v[170:171] op_sel_hi:[1,0]
	v_pk_mul_f32 v[210:211], v[114:115], v[170:171] op_sel_hi:[1,0]
	v_pk_mul_f32 v[216:217], v[130:131], v[216:217]
	v_pk_mul_f32 v[210:211], v[138:139], v[210:211]
	v_pk_mul_f32 v[212:213], v[94:95], v[170:171] op_sel_hi:[1,0]
	v_pk_mul_f32 v[214:215], v[96:97], v[170:171] op_sel_hi:[1,0]
	s_waitcnt vmcnt(3)
	v_pk_mul_f32 v[224:225], v[146:147], v[216:217]
	v_pk_mul_f32 v[218:219], v[92:93], v[170:171] op_sel_hi:[1,0]
	s_waitcnt vmcnt(1)
	v_pk_fma_f32 v[224:225], v[154:155], v[210:211], v[224:225] neg_lo:[0,0,1] neg_hi:[0,0,1]
	v_pk_mul_f32 v[154:155], v[154:155], v[216:217]
	v_pk_mul_f32 v[204:205], v[120:121], v[170:171] op_sel_hi:[1,0]
	v_pk_fma_f32 v[154:155], v[146:147], v[210:211], v[154:155]
	v_lshlrev_b32_e32 v146, 3, v229
	v_pk_mul_f32 v[206:207], v[118:119], v[170:171] op_sel_hi:[1,0]
	v_pk_mul_f32 v[208:209], v[116:117], v[170:171] op_sel_hi:[1,0]
	v_pk_mul_f32 v[214:215], v[136:137], v[214:215]
	v_pk_mul_f32 v[212:213], v[134:135], v[212:213]
	v_pk_mul_f32 v[218:219], v[132:133], v[218:219]
	v_and_b32_e32 v146, 0xf8, v146
	v_pk_mul_f32 v[206:207], v[142:143], v[206:207]
	v_pk_mul_f32 v[204:205], v[144:145], v[204:205]
	v_pk_mul_f32 v[208:209], v[140:141], v[208:209]
	v_pk_mul_f32 v[220:221], v[150:151], v[212:213]
	v_pk_mul_f32 v[222:223], v[152:153], v[214:215]
	v_pk_mul_f32 v[226:227], v[148:149], v[218:219]
	v_or3_b32 v146, v228, v146, v184
	s_waitcnt vmcnt(0)
	v_pk_fma_f32 v[222:223], v[160:161], v[204:205], v[222:223] neg_lo:[0,0,1] neg_hi:[0,0,1]
	v_pk_fma_f32 v[220:221], v[158:159], v[206:207], v[220:221] neg_lo:[0,0,1] neg_hi:[0,0,1]
	v_pk_fma_f32 v[226:227], v[156:157], v[208:209], v[226:227] neg_lo:[0,0,1] neg_hi:[0,0,1]
	v_pk_mul_f32 v[158:159], v[158:159], v[212:213]
	v_pk_mul_f32 v[160:161], v[160:161], v[214:215]
	v_pk_mul_f32 v[156:157], v[156:157], v[218:219]
	v_ashrrev_i32_e32 v147, 31, v146
	v_pk_fma_f32 v[152:153], v[152:153], v[204:205], v[160:161]
	v_pk_fma_f32 v[150:151], v[150:151], v[206:207], v[158:159]
	v_pk_fma_f32 v[156:157], v[148:149], v[208:209], v[156:157]
	v_lshl_add_u64 v[158:159], v[146:147], 1, s[54:55]
	v_cvt_pk_f16_f32 v146, v220, v221
	v_cvt_pk_f16_f32 v147, v222, v223
	v_cvt_pk_f16_f32 v148, v224, v225
	v_cvt_pk_f16_f32 v149, v226, v227
	v_bitop3_b32 v184, v199, s74, 32 bitop3:0xc8
	v_cvt_pk_f16_f32 v150, v150, v151
	v_cvt_pk_f16_f32 v151, v152, v153
	v_cvt_pk_f16_f32 v152, v154, v155
	v_cvt_pk_f16_f32 v153, v156, v157
	global_store_dwordx4 v[158:159], v[146:149], off sc1
	v_lshlrev_b32_e32 v170, 7, v184
	v_mul_f32_e32 v204, v105, v105
	v_lshl_add_u64 v[146:147], v[158:159], 0, s[10:11]
	global_store_dwordx4 v[146:147], v[150:153], off sc1
	v_lshl_add_u64 v[158:159], v[174:175], 0, v[170:171]
	v_fmac_f32_e32 v204, v104, v104
	v_lshl_add_u64 v[150:151], v[172:173], 0, v[170:171]
	global_load_dwordx4 v[146:149], v[150:151], off offset:16
	global_load_dwordx4 v[154:157], v[150:151], off
	s_nop 0
	global_load_dwordx4 v[150:153], v[158:159], off offset:16
	s_nop 0
	global_load_dwordx4 v[158:161], v[158:159], off
	v_mov_b32_e32 v247, 0
	v_add_u32_e32 v242, 0x80, v199
	v_and_b32_e32 v242, 0x7cf, v242
	v_lshlrev_b32_e32 v242, 7, v242
	v_mov_b32_e32 v246, v242
	v_lshl_add_u64 v[244:245], v[172:173], 0, v[246:247]
	global_load_dword v243, v[244:245], off
	v_lshl_add_u64 v[244:245], v[174:175], 0, v[246:247]
	global_load_dword v243, v[244:245], off
	v_add_u32_e32 v246, 0x800, v242
	v_lshl_add_u64 v[244:245], v[172:173], 0, v[246:247]
	global_load_dword v243, v[244:245], off
	v_lshl_add_u64 v[244:245], v[174:175], 0, v[246:247]
	global_load_dword v243, v[244:245], off
	v_add_u32_e32 v246, 0x1000, v242
	v_lshl_add_u64 v[244:245], v[172:173], 0, v[246:247]
	global_load_dword v243, v[244:245], off
	v_lshl_add_u64 v[244:245], v[174:175], 0, v[246:247]
	global_load_dword v243, v[244:245], off
	v_add_u32_e32 v246, 0x1800, v242
	v_lshl_add_u64 v[244:245], v[172:173], 0, v[246:247]
	global_load_dword v243, v[244:245], off
	v_lshl_add_u64 v[244:245], v[174:175], 0, v[246:247]
	global_load_dword v243, v[244:245], off
	v_mul_f32_e32 v170, v103, v103
	v_fmac_f32_e32 v170, v102, v102
	v_add_f32_e32 v170, v170, v204
	v_pk_mul_f32 v[204:205], v[100:101], v[100:101]
	v_pk_mul_f32 v[206:207], v[98:99], v[98:99]
	v_mov_b32_e32 v208, v204
	v_mov_b32_e32 v209, v206
	v_mov_b32_e32 v206, v205
	v_pk_add_f32 v[204:205], v[208:209], v[206:207]
	v_pk_mul_f32 v[206:207], v[78:79], v[78:79]
	v_add_f32_e32 v170, v170, v205
	v_add_f32_e32 v170, v204, v170
	v_pk_mul_f32 v[204:205], v[80:81], v[80:81]
	v_mov_b32_e32 v209, v206
	v_mov_b32_e32 v208, v204
	v_mov_b32_e32 v206, v205
	v_pk_add_f32 v[204:205], v[208:209], v[206:207]
	v_pk_mul_f32 v[206:207], v[74:75], v[74:75]
	v_add_f32_e32 v170, v170, v205
	v_add_f32_e32 v170, v204, v170
	v_pk_mul_f32 v[204:205], v[76:77], v[76:77]
	v_mov_b32_e32 v209, v206
	v_mov_b32_e32 v208, v204
	v_mov_b32_e32 v206, v205
	v_pk_add_f32 v[204:205], v[208:209], v[206:207]
	s_mov_b64 vcc, s[4:5]
	v_add_f32_e32 v170, v205, v170
	v_add_f32_e32 v170, v204, v170
	ds_bpermute_b32 v204, v201, v170
	v_lshlrev_b32_e32 v205, 6, v184
	s_waitcnt lgkmcnt(0)
	v_add_f32_e32 v170, v170, v204
	ds_bpermute_b32 v204, v202, v170
	s_cbranch_vccnz .LBB1_17
	v_or_b32_e32 v184, 32, v199
	v_lshlrev_b32_e32 v184, 3, v184
	v_and_b32_e32 v206, 0x1f000, v205
	v_and_b32_e32 v184, 0x178, v184
	v_or3_b32 v184, v206, v184, v203
	s_mov_b64 s[8:9], 0

.LBB1_20:
	s_waitcnt lgkmcnt(0)
	v_add_f32_e32 v170, v170, v204
	v_fmamk_f32 v170, v170, 0x3c800000, v195
	v_mul_f32_e32 v185, 0x4f800000, v170
	v_cmp_gt_f32_e32 vcc, s70, v170
	s_lshl_b32 s10, s56, 1
	v_add_u32_e32 v228, 0x80, v199
	v_cndmask_b32_e32 v170, v170, v185, vcc
	v_sqrt_f32_e32 v185, v170
	s_nop 0
	v_add_u32_e32 v204, -1, v185
	v_fma_f32 v206, -v204, v185, v170
	v_add_u32_e32 v205, 1, v185
	v_cmp_ge_f32_e64 s[4:5], 0, v206
	s_nop 1
	v_cndmask_b32_e64 v204, v185, v204, s[4:5]
	v_fma_f32 v185, -v205, v185, v170
	v_cmp_lt_f32_e64 s[4:5], 0, v185
	s_nop 1
	v_cndmask_b32_e64 v185, v204, v205, s[4:5]
	v_mul_f32_e32 v204, 0x37800000, v185
	v_cndmask_b32_e32 v185, v185, v204, vcc
	v_cmp_class_f32_e32 vcc, v170, v196
	s_nop 1
	v_cndmask_b32_e32 v170, v185, v170, vcc
	v_div_scale_f32 v185, s[4:5], v170, v170, v200
	v_rcp_f32_e32 v204, v185
	s_nop 0
	v_fma_f32 v205, -v185, v204, 1.0
	v_fmac_f32_e32 v204, v205, v204
	v_div_scale_f32 v205, vcc, v200, v170, v200
	v_mul_f32_e32 v206, v205, v204
	v_fma_f32 v207, -v185, v206, v205
	v_fmac_f32_e32 v206, v207, v204
	v_fma_f32 v185, -v185, v206, v205
	v_div_fmas_f32 v185, v185, v204, v206
	v_div_fixup_f32 v170, v185, v170, v200
	v_pk_mul_f32 v[212:213], v[78:79], v[170:171] op_sel_hi:[1,0]
	v_pk_mul_f32 v[214:215], v[80:81], v[170:171] op_sel_hi:[1,0]
	v_pk_mul_f32 v[216:217], v[74:75], v[170:171] op_sel_hi:[1,0]
	v_pk_mul_f32 v[218:219], v[76:77], v[170:171] op_sel_hi:[1,0]
	v_pk_mul_f32 v[204:205], v[104:105], v[170:171] op_sel_hi:[1,0]
	v_pk_mul_f32 v[206:207], v[102:103], v[170:171] op_sel_hi:[1,0]
	v_pk_mul_f32 v[208:209], v[100:101], v[170:171] op_sel_hi:[1,0]
	v_pk_mul_f32 v[210:211], v[98:99], v[170:171] op_sel_hi:[1,0]
	v_pk_mul_f32 v[214:215], v[136:137], v[214:215]
	v_pk_mul_f32 v[212:213], v[134:135], v[212:213]
	v_pk_mul_f32 v[218:219], v[132:133], v[218:219]
	v_pk_mul_f32 v[216:217], v[130:131], v[216:217]
	v_pk_mul_f32 v[206:207], v[142:143], v[206:207]
	v_pk_mul_f32 v[204:205], v[144:145], v[204:205]
	v_pk_mul_f32 v[210:211], v[138:139], v[210:211]
	v_pk_mul_f32 v[208:209], v[140:141], v[208:209]
	s_waitcnt vmcnt(8)
	v_pk_mul_f32 v[220:221], v[158:159], v[212:213]
	v_pk_mul_f32 v[222:223], v[160:161], v[214:215]
	v_pk_mul_f32 v[224:225], v[150:151], v[216:217]
	v_pk_mul_f32 v[226:227], v[152:153], v[218:219]
	v_pk_fma_f32 v[222:223], v[156:157], v[204:205], v[222:223] neg_lo:[0,0,1] neg_hi:[0,0,1]
	v_pk_fma_f32 v[220:221], v[154:155], v[206:207], v[220:221] neg_lo:[0,0,1] neg_hi:[0,0,1]
	v_pk_fma_f32 v[226:227], v[148:149], v[208:209], v[226:227] neg_lo:[0,0,1] neg_hi:[0,0,1]
	v_pk_fma_f32 v[224:225], v[146:147], v[210:211], v[224:225] neg_lo:[0,0,1] neg_hi:[0,0,1]
	v_pk_mul_f32 v[154:155], v[154:155], v[212:213]
	v_pk_mul_f32 v[156:157], v[156:157], v[214:215]
	v_pk_mul_f32 v[146:147], v[146:147], v[216:217]
	v_pk_mul_f32 v[148:149], v[148:149], v[218:219]
	v_ashrrev_i32_e32 v185, 31, v184
	v_pk_fma_f32 v[156:157], v[160:161], v[204:205], v[156:157]
	v_pk_fma_f32 v[154:155], v[158:159], v[206:207], v[154:155]
	v_pk_fma_f32 v[158:159], v[152:153], v[208:209], v[148:149]
	v_pk_fma_f32 v[152:153], v[150:151], v[210:211], v[146:147]
	v_lshl_add_u64 v[160:161], v[184:185], 1, s[8:9]
	v_cvt_pk_f16_f32 v146, v220, v221
	v_cvt_pk_f16_f32 v147, v222, v223
	v_cvt_pk_f16_f32 v148, v224, v225
	v_cvt_pk_f16_f32 v149, v226, v227
	v_cvt_pk_f16_f32 v150, v154, v155
	v_cvt_pk_f16_f32 v151, v156, v157
	v_cvt_pk_f16_f32 v152, v152, v153
	v_cvt_pk_f16_f32 v153, v158, v159
	global_store_dwordx4 v[160:161], v[146:149], off sc1
	v_bitop3_b32 v226, v199, s75, 48 bitop3:0xc8
	v_lshlrev_b32_e32 v170, 7, v226
	v_lshl_add_u64 v[146:147], v[160:161], 0, s[10:11]
	global_store_dwordx4 v[146:147], v[150:153], off sc1
	v_mul_f32_e32 v146, v87, v87
	v_mul_f32_e32 v147, v89, v89
	v_fmac_f32_e32 v146, v86, v86
	v_fmac_f32_e32 v147, v88, v88
	v_add_f32_e32 v152, v146, v147
	v_pk_mul_f32 v[146:147], v[84:85], v[84:85]
	v_pk_mul_f32 v[148:149], v[82:83], v[82:83]
	v_mov_b32_e32 v150, v146
	v_mov_b32_e32 v151, v148
	v_mov_b32_e32 v148, v147
	v_pk_add_f32 v[146:147], v[150:151], v[148:149]
	v_lshl_add_u64 v[158:159], v[172:173], 0, v[170:171]
	v_add_f32_e32 v147, v152, v147
	v_lshl_add_u64 v[150:151], v[174:175], 0, v[170:171]
	v_add_f32_e32 v208, v146, v147
	global_load_dwordx4 v[146:149], v[150:151], off offset:16
	s_nop 0
	global_load_dwordx4 v[150:153], v[150:151], off
	s_nop 0
	global_load_dwordx4 v[154:157], v[158:159], off offset:16
	s_nop 0
	global_load_dwordx4 v[158:161], v[158:159], off
	v_pk_mul_f32 v[184:185], v[72:73], v[72:73]
	v_pk_mul_f32 v[204:205], v[70:71], v[70:71]
	v_mov_b32_e32 v206, v184
	v_mov_b32_e32 v207, v204
	v_mov_b32_e32 v204, v185
	v_pk_add_f32 v[184:185], v[206:207], v[204:205]
	v_pk_mul_f32 v[204:205], v[66:67], v[66:67]
	v_add_f32_e32 v170, v208, v185
	v_add_f32_e32 v170, v184, v170
	v_pk_mul_f32 v[184:185], v[68:69], v[68:69]
	v_mov_b32_e32 v207, v204
	v_mov_b32_e32 v206, v184
	v_mov_b32_e32 v204, v185
	v_pk_add_f32 v[184:185], v[206:207], v[204:205]
	v_or_b32_e32 v227, 48, v199
	v_add_f32_e32 v170, v185, v170
	v_add_f32_e32 v170, v184, v170
	ds_bpermute_b32 v184, v201, v170
	s_waitcnt lgkmcnt(0)
	v_add_f32_e32 v170, v170, v184
	ds_bpermute_b32 v184, v202, v170
	s_waitcnt lgkmcnt(0)
	v_add_f32_e32 v170, v170, v184
	v_fmamk_f32 v170, v170, 0x3c800000, v195
	v_mul_f32_e32 v184, 0x4f800000, v170
	v_cmp_gt_f32_e32 vcc, s70, v170
	s_nop 1
	v_cndmask_b32_e32 v170, v170, v184, vcc
	v_sqrt_f32_e32 v184, v170
	s_nop 0
	v_add_u32_e32 v185, -1, v184
	v_fma_f32 v204, -v185, v184, v170
	v_cmp_ge_f32_e64 s[4:5], 0, v204
	v_add_u32_e32 v204, 1, v184
	s_nop 0
	v_cndmask_b32_e64 v185, v184, v185, s[4:5]
	v_fma_f32 v184, -v204, v184, v170
	v_cmp_lt_f32_e64 s[4:5], 0, v184
	s_nop 1
	v_cndmask_b32_e64 v184, v185, v204, s[4:5]
	v_mul_f32_e32 v185, 0x37800000, v184
	v_cndmask_b32_e32 v184, v184, v185, vcc
	v_cmp_class_f32_e32 vcc, v170, v196
	s_nop 1
	v_cndmask_b32_e32 v170, v184, v170, vcc
	v_div_scale_f32 v184, s[4:5], v170, v170, v200
	v_rcp_f32_e32 v185, v184
	s_nop 0
	v_fma_f32 v204, -v184, v185, 1.0
	v_fmac_f32_e32 v185, v204, v185
	v_div_scale_f32 v204, vcc, v200, v170, v200
	v_mul_f32_e32 v205, v204, v185
	v_fma_f32 v206, -v184, v205, v204
	v_fmac_f32_e32 v205, v206, v185
	v_fma_f32 v184, -v184, v205, v204
	v_div_fmas_f32 v184, v184, v185, v205
	v_div_fixup_f32 v170, v184, v170, v200
	v_pk_mul_f32 v[214:215], v[66:67], v[170:171] op_sel_hi:[1,0]
	v_pk_mul_f32 v[208:209], v[82:83], v[170:171] op_sel_hi:[1,0]
	v_pk_mul_f32 v[214:215], v[130:131], v[214:215]
	v_pk_mul_f32 v[208:209], v[138:139], v[208:209]
	s_waitcnt vmcnt(3)
	v_pk_mul_f32 v[222:223], v[146:147], v[214:215]
	v_pk_mul_f32 v[210:211], v[70:71], v[170:171] op_sel_hi:[1,0]
	s_waitcnt vmcnt(1)
	v_pk_fma_f32 v[222:223], v[154:155], v[208:209], v[222:223] neg_lo:[0,0,1] neg_hi:[0,0,1]
	v_pk_mul_f32 v[154:155], v[154:155], v[214:215]
	v_pk_mul_f32 v[212:213], v[72:73], v[170:171] op_sel_hi:[1,0]
	v_pk_mul_f32 v[216:217], v[68:69], v[170:171] op_sel_hi:[1,0]
	v_pk_fma_f32 v[154:155], v[146:147], v[208:209], v[154:155]
	v_lshlrev_b32_e32 v146, 6, v226
	v_lshlrev_b32_e32 v147, 3, v227
	v_pk_mul_f32 v[184:185], v[88:89], v[170:171] op_sel_hi:[1,0]
	v_pk_mul_f32 v[204:205], v[86:87], v[170:171] op_sel_hi:[1,0]
	v_pk_mul_f32 v[206:207], v[84:85], v[170:171] op_sel_hi:[1,0]
	v_pk_mul_f32 v[212:213], v[136:137], v[212:213]
	v_pk_mul_f32 v[210:211], v[134:135], v[210:211]
	v_pk_mul_f32 v[216:217], v[132:133], v[216:217]
	v_and_b32_e32 v146, s79, v146
	v_and_b32_e32 v147, s57, v147
	v_pk_mul_f32 v[204:205], v[142:143], v[204:205]
	v_pk_mul_f32 v[184:185], v[144:145], v[184:185]
	v_pk_mul_f32 v[206:207], v[140:141], v[206:207]
	v_pk_mul_f32 v[218:219], v[150:151], v[210:211]
	v_pk_mul_f32 v[220:221], v[152:153], v[212:213]
	v_pk_mul_f32 v[224:225], v[148:149], v[216:217]
	v_or3_b32 v146, v147, v203, v146
	s_waitcnt vmcnt(0)
	v_pk_fma_f32 v[220:221], v[160:161], v[184:185], v[220:221] neg_lo:[0,0,1] neg_hi:[0,0,1]
	v_pk_fma_f32 v[218:219], v[158:159], v[204:205], v[218:219] neg_lo:[0,0,1] neg_hi:[0,0,1]
	v_pk_fma_f32 v[224:225], v[156:157], v[206:207], v[224:225] neg_lo:[0,0,1] neg_hi:[0,0,1]
	v_pk_mul_f32 v[158:159], v[158:159], v[210:211]
	v_pk_mul_f32 v[160:161], v[160:161], v[212:213]
	v_pk_mul_f32 v[156:157], v[156:157], v[216:217]
	v_ashrrev_i32_e32 v147, 31, v146
	v_pk_fma_f32 v[152:153], v[152:153], v[184:185], v[160:161]
	v_pk_fma_f32 v[150:151], v[150:151], v[204:205], v[158:159]
	v_pk_fma_f32 v[156:157], v[148:149], v[206:207], v[156:157]
	v_lshl_add_u64 v[158:159], v[146:147], 1, s[8:9]
	v_cvt_pk_f16_f32 v146, v218, v219
	v_cvt_pk_f16_f32 v147, v220, v221
	v_cvt_pk_f16_f32 v148, v222, v223
	v_cvt_pk_f16_f32 v149, v224, v225
	v_cvt_pk_f16_f32 v150, v150, v151
	v_cvt_pk_f16_f32 v151, v152, v153
	v_cvt_pk_f16_f32 v152, v154, v155
	v_cvt_pk_f16_f32 v153, v156, v157
	global_store_dwordx4 v[158:159], v[146:149], off sc1
	v_pk_mul_f32 v[184:185], v[48:49], v[48:49]
	v_pk_mul_f32 v[204:205], v[46:47], v[46:47]
	v_lshl_add_u64 v[146:147], v[158:159], 0, s[10:11]
	global_store_dwordx4 v[146:147], v[150:153], off sc1
	v_mul_f32_e32 v146, v63, v63
	v_mul_f32_e32 v147, v65, v65
	v_fmac_f32_e32 v146, v62, v62
	v_fmac_f32_e32 v147, v64, v64
	v_add_f32_e32 v153, v146, v147
	v_pk_mul_f32 v[146:147], v[60:61], v[60:61]
	v_pk_mul_f32 v[148:149], v[58:59], v[58:59]
	v_and_b32_e32 v152, 0x7cf, v228
	v_mov_b32_e32 v150, v146
	v_mov_b32_e32 v151, v148
	v_mov_b32_e32 v148, v147
	v_pk_add_f32 v[146:147], v[150:151], v[148:149]
	v_lshlrev_b32_e32 v170, 7, v152
	v_add_f32_e32 v147, v153, v147
	v_lshl_add_u64 v[158:159], v[172:173], 0, v[170:171]
	v_lshl_add_u64 v[150:151], v[174:175], 0, v[170:171]
	v_add_f32_e32 v203, v146, v147
	global_load_dwordx4 v[146:149], v[150:151], off offset:16
	s_nop 0
	global_load_dwordx4 v[150:153], v[150:151], off
	s_nop 0
	global_load_dwordx4 v[154:157], v[158:159], off offset:16
	s_nop 0
	global_load_dwordx4 v[158:161], v[158:159], off
	v_mov_b32_e32 v206, v184
	v_mov_b32_e32 v207, v204
	v_mov_b32_e32 v204, v185
	v_pk_add_f32 v[184:185], v[206:207], v[204:205]
	v_pk_mul_f32 v[204:205], v[42:43], v[42:43]
	v_add_f32_e32 v170, v203, v185
	v_add_f32_e32 v170, v184, v170
	v_pk_mul_f32 v[184:185], v[44:45], v[44:45]
	v_mov_b32_e32 v207, v204
	v_mov_b32_e32 v206, v184
	v_mov_b32_e32 v204, v185
	v_pk_add_f32 v[184:185], v[206:207], v[204:205]
	s_nop 0
	v_add_f32_e32 v170, v185, v170
	v_add_f32_e32 v170, v184, v170
	ds_bpermute_b32 v184, v201, v170
	v_lshrrev_b32_e32 v185, 8, v228
	v_and_b32_e32 v185, 0x7ff8, v185
	v_add_u32_e32 v185, s78, v185
	v_lshl_or_b32 v203, v185, 17, v187
	s_waitcnt lgkmcnt(0)
	v_add_f32_e32 v170, v170, v184
	ds_bpermute_b32 v184, v202, v170
	v_lshrrev_b32_e32 v185, 6, v228
	v_and_b32_e32 v185, 0x7fe0, v185
	v_add_u32_e32 v185, s37, v185
	v_lshl_or_b32 v185, v185, 17, v188
	s_waitcnt lgkmcnt(0)
	v_add_f32_e32 v170, v170, v184
	v_fmamk_f32 v170, v170, 0x3c800000, v195
	v_mul_f32_e32 v184, 0x4f800000, v170
	v_cmp_gt_f32_e32 vcc, s70, v170
	s_nop 1
	v_cndmask_b32_e32 v170, v170, v184, vcc
	v_sqrt_f32_e32 v184, v170
	s_nop 0
	v_add_u32_e32 v204, -1, v184
	v_fma_f32 v205, -v204, v184, v170
	v_cmp_ge_f32_e64 s[4:5], 0, v205
	v_add_u32_e32 v205, 1, v184
	s_nop 0
	v_cndmask_b32_e64 v204, v184, v204, s[4:5]
	v_fma_f32 v184, -v205, v184, v170
	v_cmp_lt_f32_e64 s[4:5], 0, v184
	s_nop 1
	v_cndmask_b32_e64 v184, v204, v205, s[4:5]
	v_mul_f32_e32 v204, 0x37800000, v184
	v_cndmask_b32_e32 v184, v184, v204, vcc
	v_cmp_class_f32_e32 vcc, v170, v196
	s_nop 1
	v_cndmask_b32_e32 v170, v184, v170, vcc
	v_div_scale_f32 v184, s[4:5], v170, v170, v200
	v_rcp_f32_e32 v204, v184
	s_nop 0
	v_fma_f32 v205, -v184, v204, 1.0
	v_fmac_f32_e32 v204, v205, v204
	v_div_scale_f32 v205, vcc, v200, v170, v200
	v_mul_f32_e32 v206, v205, v204
	v_fma_f32 v207, -v184, v206, v205
	v_fmac_f32_e32 v206, v207, v204
	v_fma_f32 v184, -v184, v206, v205
	v_div_fmas_f32 v184, v184, v204, v206
	v_div_fixup_f32 v170, v184, v170, v200
	v_pk_mul_f32 v[216:217], v[42:43], v[170:171] op_sel_hi:[1,0]
	v_pk_mul_f32 v[210:211], v[58:59], v[170:171] op_sel_hi:[1,0]
	v_pk_mul_f32 v[216:217], v[130:131], v[216:217]
	v_pk_mul_f32 v[210:211], v[138:139], v[210:211]
	v_pk_mul_f32 v[212:213], v[46:47], v[170:171] op_sel_hi:[1,0]
	v_pk_mul_f32 v[214:215], v[48:49], v[170:171] op_sel_hi:[1,0]
	s_waitcnt vmcnt(3)
	v_pk_mul_f32 v[224:225], v[146:147], v[216:217]
	v_pk_mul_f32 v[218:219], v[44:45], v[170:171] op_sel_hi:[1,0]
	s_waitcnt vmcnt(1)
	v_pk_fma_f32 v[224:225], v[154:155], v[210:211], v[224:225] neg_lo:[0,0,1] neg_hi:[0,0,1]
	v_pk_mul_f32 v[154:155], v[154:155], v[216:217]
	v_pk_mul_f32 v[204:205], v[64:65], v[170:171] op_sel_hi:[1,0]
	v_pk_fma_f32 v[154:155], v[146:147], v[210:211], v[154:155]
	v_lshlrev_b32_e32 v146, 6, v228
	v_pk_mul_f32 v[206:207], v[62:63], v[170:171] op_sel_hi:[1,0]
	v_pk_mul_f32 v[208:209], v[60:61], v[170:171] op_sel_hi:[1,0]
	v_pk_mul_f32 v[214:215], v[136:137], v[214:215]
	v_pk_mul_f32 v[212:213], v[134:135], v[212:213]
	v_pk_mul_f32 v[218:219], v[132:133], v[218:219]
	v_cndmask_b32_e64 v184, v203, v185, s[6:7]
	v_and_b32_e32 v146, 0x1f000, v146
	v_pk_mul_f32 v[206:207], v[142:143], v[206:207]
	v_pk_mul_f32 v[204:205], v[144:145], v[204:205]
	v_pk_mul_f32 v[208:209], v[140:141], v[208:209]
	v_pk_mul_f32 v[220:221], v[150:151], v[212:213]
	v_pk_mul_f32 v[222:223], v[152:153], v[214:215]
	v_pk_mul_f32 v[226:227], v[148:149], v[218:219]
	v_or3_b32 v146, v146, v189, v184
	s_waitcnt vmcnt(0)
	v_pk_fma_f32 v[222:223], v[160:161], v[204:205], v[222:223] neg_lo:[0,0,1] neg_hi:[0,0,1]
	v_pk_fma_f32 v[220:221], v[158:159], v[206:207], v[220:221] neg_lo:[0,0,1] neg_hi:[0,0,1]
	v_pk_fma_f32 v[226:227], v[156:157], v[208:209], v[226:227] neg_lo:[0,0,1] neg_hi:[0,0,1]
	v_pk_mul_f32 v[158:159], v[158:159], v[212:213]
	v_pk_mul_f32 v[160:161], v[160:161], v[214:215]
	v_pk_mul_f32 v[156:157], v[156:157], v[218:219]
	v_ashrrev_i32_e32 v147, 31, v146
	v_pk_fma_f32 v[152:153], v[152:153], v[204:205], v[160:161]
	v_pk_fma_f32 v[150:151], v[150:151], v[206:207], v[158:159]
	v_pk_fma_f32 v[156:157], v[148:149], v[208:209], v[156:157]
	v_lshl_add_u64 v[158:159], v[146:147], 1, s[54:55]
	v_cvt_pk_f16_f32 v146, v220, v221
	v_cvt_pk_f16_f32 v147, v222, v223
	v_cvt_pk_f16_f32 v148, v224, v225
	v_cvt_pk_f16_f32 v149, v226, v227
	v_cvt_pk_f16_f32 v150, v150, v151
	v_cvt_pk_f16_f32 v151, v152, v153
	v_cvt_pk_f16_f32 v152, v154, v155
	v_cvt_pk_f16_f32 v153, v156, v157
	global_store_dwordx4 v[158:159], v[146:149], off sc1
	v_add_u32_e32 v228, 0x90, v199
	v_pk_mul_f32 v[204:205], v[32:33], v[32:33]
	v_lshl_add_u64 v[146:147], v[158:159], 0, s[10:11]
	global_store_dwordx4 v[146:147], v[150:153], off sc1
	v_mul_f32_e32 v146, v55, v55
	v_mul_f32_e32 v147, v57, v57
	v_fmac_f32_e32 v146, v54, v54
	v_fmac_f32_e32 v147, v56, v56
	v_add_f32_e32 v153, v146, v147
	v_pk_mul_f32 v[146:147], v[52:53], v[52:53]
	v_pk_mul_f32 v[148:149], v[50:51], v[50:51]
	v_and_b32_e32 v152, 0x7df, v228
	v_mov_b32_e32 v150, v146
	v_mov_b32_e32 v151, v148
	v_mov_b32_e32 v148, v147
	v_pk_add_f32 v[146:147], v[150:151], v[148:149]
	v_lshlrev_b32_e32 v170, 7, v152
	v_add_f32_e32 v147, v153, v147
	v_lshl_add_u64 v[158:159], v[172:173], 0, v[170:171]
	v_lshl_add_u64 v[150:151], v[174:175], 0, v[170:171]
	v_add_f32_e32 v210, v146, v147
	global_load_dwordx4 v[146:149], v[150:151], off offset:16
	s_nop 0
	global_load_dwordx4 v[150:153], v[150:151], off
	s_nop 0
	global_load_dwordx4 v[154:157], v[158:159], off offset:16
	s_nop 0
	global_load_dwordx4 v[158:161], v[158:159], off
	v_pk_mul_f32 v[206:207], v[30:31], v[30:31]
	v_mov_b32_e32 v208, v204
	v_mov_b32_e32 v209, v206
	v_mov_b32_e32 v206, v205
	v_pk_add_f32 v[204:205], v[208:209], v[206:207]
	v_pk_mul_f32 v[206:207], v[26:27], v[26:27]
	v_add_f32_e32 v170, v210, v205
	v_add_f32_e32 v170, v204, v170
	v_pk_mul_f32 v[204:205], v[28:29], v[28:29]
	v_mov_b32_e32 v209, v206
	v_mov_b32_e32 v208, v204
	v_mov_b32_e32 v206, v205
	v_pk_add_f32 v[204:205], v[208:209], v[206:207]
	s_nop 0
	v_add_f32_e32 v170, v205, v170
	v_add_f32_e32 v170, v204, v170
	ds_bpermute_b32 v204, v201, v170
	s_waitcnt lgkmcnt(0)
	v_add_f32_e32 v170, v170, v204
	ds_bpermute_b32 v204, v202, v170
	s_waitcnt lgkmcnt(0)
	v_add_f32_e32 v170, v170, v204
	v_fmamk_f32 v170, v170, 0x3c800000, v195
	v_mul_f32_e32 v204, 0x4f800000, v170
	v_cmp_gt_f32_e32 vcc, s70, v170
	s_nop 1
	v_cndmask_b32_e32 v170, v170, v204, vcc
	v_sqrt_f32_e32 v204, v170
	s_nop 0
	v_add_u32_e32 v205, -1, v204
	v_fma_f32 v206, -v205, v204, v170
	v_cmp_ge_f32_e64 s[4:5], 0, v206
	v_add_u32_e32 v206, 1, v204
	s_nop 0
	v_cndmask_b32_e64 v205, v204, v205, s[4:5]
	v_fma_f32 v204, -v206, v204, v170
	v_cmp_lt_f32_e64 s[4:5], 0, v204
	s_nop 1
	v_cndmask_b32_e64 v204, v205, v206, s[4:5]
	v_mul_f32_e32 v205, 0x37800000, v204
	v_cndmask_b32_e32 v204, v204, v205, vcc
	v_cmp_class_f32_e32 vcc, v170, v196
	s_nop 1
	v_cndmask_b32_e32 v170, v204, v170, vcc
	v_div_scale_f32 v204, s[4:5], v170, v170, v200
	v_rcp_f32_e32 v205, v204
	s_mov_b64 s[4:5], -1
	v_fma_f32 v206, -v204, v205, 1.0
	v_fmac_f32_e32 v205, v206, v205
	v_div_scale_f32 v206, vcc, v200, v170, v200
	v_mul_f32_e32 v207, v206, v205
	v_fma_f32 v208, -v204, v207, v206
	v_fmac_f32_e32 v207, v208, v205
	v_fma_f32 v204, -v204, v207, v206
	v_div_fmas_f32 v204, v204, v205, v207
	v_div_fixup_f32 v170, v204, v170, v200
	v_pk_mul_f32 v[216:217], v[26:27], v[170:171] op_sel_hi:[1,0]
	v_pk_mul_f32 v[210:211], v[50:51], v[170:171] op_sel_hi:[1,0]
	v_pk_mul_f32 v[216:217], v[130:131], v[216:217]
	v_pk_mul_f32 v[210:211], v[138:139], v[210:211]
	v_pk_mul_f32 v[214:215], v[32:33], v[170:171] op_sel_hi:[1,0]
	s_waitcnt vmcnt(3)
	v_pk_mul_f32 v[224:225], v[146:147], v[216:217]
	v_pk_mul_f32 v[204:205], v[56:57], v[170:171] op_sel_hi:[1,0]
	s_waitcnt vmcnt(1)
	v_pk_fma_f32 v[224:225], v[154:155], v[210:211], v[224:225] neg_lo:[0,0,1] neg_hi:[0,0,1]
	v_pk_mul_f32 v[154:155], v[154:155], v[216:217]
	v_pk_mul_f32 v[212:213], v[30:31], v[170:171] op_sel_hi:[1,0]
	v_pk_mul_f32 v[214:215], v[136:137], v[214:215]
	v_pk_mul_f32 v[218:219], v[28:29], v[170:171] op_sel_hi:[1,0]
	v_pk_fma_f32 v[154:155], v[146:147], v[210:211], v[154:155]
	v_lshlrev_b32_e32 v146, 6, v228
	v_lshlrev_b32_e32 v147, 3, v228
	v_pk_mul_f32 v[206:207], v[54:55], v[170:171] op_sel_hi:[1,0]
	v_pk_mul_f32 v[204:205], v[144:145], v[204:205]
	v_pk_mul_f32 v[208:209], v[52:53], v[170:171] op_sel_hi:[1,0]
	v_pk_mul_f32 v[212:213], v[134:135], v[212:213]
	v_pk_mul_f32 v[218:219], v[132:133], v[218:219]
	v_pk_mul_f32 v[222:223], v[152:153], v[214:215]
	v_and_b32_e32 v146, 0x1f000, v146
	v_and_b32_e32 v147, 0xf8, v147
	v_pk_mul_f32 v[206:207], v[142:143], v[206:207]
	v_pk_mul_f32 v[208:209], v[140:141], v[208:209]
	v_pk_mul_f32 v[220:221], v[150:151], v[212:213]
	s_waitcnt vmcnt(0)
	v_pk_fma_f32 v[222:223], v[160:161], v[204:205], v[222:223] neg_lo:[0,0,1] neg_hi:[0,0,1]
	v_pk_mul_f32 v[226:227], v[148:149], v[218:219]
	v_pk_mul_f32 v[160:161], v[160:161], v[214:215]
	v_or3_b32 v146, v146, v147, v184
	v_pk_fma_f32 v[220:221], v[158:159], v[206:207], v[220:221] neg_lo:[0,0,1] neg_hi:[0,0,1]
	v_pk_fma_f32 v[226:227], v[156:157], v[208:209], v[226:227] neg_lo:[0,0,1] neg_hi:[0,0,1]
	v_pk_mul_f32 v[158:159], v[158:159], v[212:213]
	v_pk_fma_f32 v[152:153], v[152:153], v[204:205], v[160:161]
	v_pk_mul_f32 v[156:157], v[156:157], v[218:219]
	v_ashrrev_i32_e32 v147, 31, v146
	v_add_u32_e32 v204, 0xa0, v199
	v_pk_fma_f32 v[150:151], v[150:151], v[206:207], v[158:159]
	v_pk_fma_f32 v[156:157], v[148:149], v[208:209], v[156:157]
	v_lshl_add_u64 v[158:159], v[146:147], 1, s[54:55]
	v_cvt_pk_f16_f32 v146, v220, v221
	v_cvt_pk_f16_f32 v147, v222, v223
	v_cvt_pk_f16_f32 v148, v224, v225
	v_cvt_pk_f16_f32 v149, v226, v227
	v_and_b32_e32 v184, 0x7ef, v204
	v_cvt_pk_f16_f32 v150, v150, v151
	v_cvt_pk_f16_f32 v151, v152, v153
	v_cvt_pk_f16_f32 v152, v154, v155
	v_cvt_pk_f16_f32 v153, v156, v157
	global_store_dwordx4 v[158:159], v[146:149], off sc1
	v_lshlrev_b32_e32 v170, 7, v184
	v_mul_f32_e32 v205, v41, v41
	v_lshl_add_u64 v[146:147], v[158:159], 0, s[10:11]
	global_store_dwordx4 v[146:147], v[150:153], off sc1
	v_lshl_add_u64 v[158:159], v[174:175], 0, v[170:171]
	v_pk_mul_f32 v[206:207], v[36:37], v[36:37]
	v_lshl_add_u64 v[150:151], v[172:173], 0, v[170:171]
	global_load_dwordx4 v[146:149], v[150:151], off offset:16
	global_load_dwordx4 v[154:157], v[150:151], off
	s_nop 0
	global_load_dwordx4 v[150:153], v[158:159], off offset:16
	s_nop 0
	global_load_dwordx4 v[158:161], v[158:159], off
	v_mul_f32_e32 v170, v39, v39
	v_pk_mul_f32 v[208:209], v[34:35], v[34:35]
	v_fmac_f32_e32 v170, v38, v38
	v_fmac_f32_e32 v205, v40, v40
	v_mov_b32_e32 v210, v206
	v_mov_b32_e32 v211, v208
	v_mov_b32_e32 v208, v207
	v_add_f32_e32 v170, v170, v205
	v_pk_add_f32 v[206:207], v[210:211], v[208:209]
	v_pk_mul_f32 v[208:209], v[14:15], v[14:15]
	v_add_f32_e32 v170, v170, v207
	v_add_f32_e32 v170, v206, v170
	v_pk_mul_f32 v[206:207], v[16:17], v[16:17]
	v_mov_b32_e32 v211, v208
	v_mov_b32_e32 v210, v206
	v_mov_b32_e32 v208, v207
	v_pk_add_f32 v[206:207], v[210:211], v[208:209]
	v_pk_mul_f32 v[208:209], v[10:11], v[10:11]
	v_add_f32_e32 v170, v170, v207
	v_add_f32_e32 v170, v206, v170
	v_pk_mul_f32 v[206:207], v[12:13], v[12:13]
	v_mov_b32_e32 v211, v208
	v_mov_b32_e32 v210, v206
	v_mov_b32_e32 v208, v207
	v_pk_add_f32 v[206:207], v[210:211], v[208:209]
	s_andn2_b64 vcc, exec, s[52:53]
	v_add_f32_e32 v170, v207, v170
	v_add_f32_e32 v170, v206, v170
	ds_bpermute_b32 v205, v201, v170
	v_lshlrev_b32_e32 v206, 6, v184
	s_waitcnt lgkmcnt(0)
	v_add_f32_e32 v170, v170, v205
	ds_bpermute_b32 v205, v202, v170
	s_cbranch_vccnz .LBB1_22
	v_lshlrev_b32_e32 v204, 3, v204
	v_and_b32_e32 v184, 0x1f000, v206
	v_and_b32_e32 v204, 0x178, v204
	v_or3_b32 v184, v184, v204, v203
	s_mov_b64 s[4:5], 0
